# tail top-4 selection: the 4 partial-logit LDS reads issued together (counted waits), cross-row lane^16 exchange via v_permlane16_swap + select instead of ds_bpermute round trips
# speedup vs baseline: 1.0179x; 1.0044x over previous
; DI int shfl_src(int x, int src_lane) { return __builtin_amdgcn_ds_bpermute(src_lane << 2, x); }
; DI void phase_tail(const Frame& F, int l) {
;     ...
;             const int tkl = 4 * F.wave + 2 * it + h, t = 32 * ti + tkl;
;             float mylogit = rb;
; #pragma unroll
;             for (int w = 0; w < 8; ++w) mylogit += Pz[(w * 32 + tkl) * 32 + r];
;             float tv[4]; int tix[4];
; #pragma unroll
;             for (int k = 0; k < 4; ++k) { float v = mylogit; int idx = r;
; #pragma unroll
;                 for (int st = 0; st < 5; ++st) { float ov; int oi;
;                     if (st == 0) { ov = __builtin_bit_cast(float, __builtin_amdgcn_update_dpp(0, __builtin_bit_cast(int, v), 0xB1, 0xf, 0xf, true)); oi = __builtin_amdgcn_update_dpp(0, idx, 0xB1, 0xf, 0xf, true); }
;                     else if (st == 1) { ov = __builtin_bit_cast(float, __builtin_amdgcn_update_dpp(0, __builtin_bit_cast(int, v), 0x4E, 0xf, 0xf, true)); oi = __builtin_amdgcn_update_dpp(0, idx, 0x4E, 0xf, 0xf, true); }
;                     else if (st == 2) { ov = __builtin_bit_cast(float, __builtin_amdgcn_update_dpp(0, __builtin_bit_cast(int, v), 0x141, 0xf, 0xf, true)); oi = __builtin_amdgcn_update_dpp(0, idx, 0x141, 0xf, 0xf, true); }
;                     else if (st == 3) { ov = __builtin_bit_cast(float, __builtin_amdgcn_update_dpp(0, __builtin_bit_cast(int, v), 0x140, 0xf, 0xf, true)); oi = __builtin_amdgcn_update_dpp(0, idx, 0x140, 0xf, 0xf, true); }
;                     else { ov = __builtin_bit_cast(float, shfl_src(__builtin_bit_cast(int, v), F.lane ^ 16)); oi = shfl_src(idx, F.lane ^ 16); }
;                     if (ov > v || (ov == v && oi < idx)) { v = ov; idx = oi; } }
;                 tv[k] = v; tix[k] = idx; if (r == idx) mylogit = neg_big; }
.LBB0_963:
	v_or_b32_e32 v0, s2, v138
	v_lshl_add_u32 v1, v0, 7, v137
	ds_read2st64_b32 v[2:3], v1 offset1:16
	ds_read2st64_b32 v[100:101], v1 offset0:32 offset1:48
	ds_read2st64_b32 v[102:103], v1 offset0:64 offset1:80
	ds_read2st64_b32 v[104:105], v1 offset0:96 offset1:112
	s_mov_b32 s70, 0xffff
	s_mov_b32 s71, 0xffff
	v_mov_b32_dpp v6, v67 quad_perm:[1,0,3,2] row_mask:0xf bank_mask:0xf bound_ctrl:1
	s_waitcnt lgkmcnt(3)
	v_add_f32_e32 v2, v135, v2
	v_add_f32_e32 v4, v2, v3
	s_waitcnt lgkmcnt(2)
	v_add_f32_e32 v2, v4, v100
	v_add_f32_e32 v4, v2, v101
	s_waitcnt lgkmcnt(1)
	v_add_f32_e32 v2, v4, v102
	v_add_f32_e32 v4, v2, v103
	s_waitcnt lgkmcnt(0)
	v_add_f32_e32 v1, v4, v104
	v_add_f32_e32 v3, v1, v105
	s_nop 1
	v_mov_b32_dpp v4, v3 quad_perm:[1,0,3,2] row_mask:0xf bank_mask:0xf bound_ctrl:1
	v_cmp_lt_f32_e64 s[4:5], v3, v4
	v_cmp_nlt_f32_e32 vcc, v3, v4
	s_and_saveexec_b64 s[6:7], vcc
	v_cmp_eq_f32_e32 vcc, v3, v4
	v_cmp_lt_i32_e64 s[46:47], v6, v67
	s_and_b64 s[12:13], vcc, s[46:47]
	s_andn2_b64 s[4:5], s[4:5], exec
	s_and_b64 s[12:13], s[12:13], exec
	s_or_b64 s[4:5], s[4:5], s[12:13]
	s_or_b64 exec, exec, s[6:7]
	v_mov_b32_e32 v5, v3
	v_mov_b32_e32 v2, v3
	v_mov_b32_e32 v1, v67
	s_and_saveexec_b64 s[6:7], s[4:5]
	v_mov_b32_e32 v5, v4
	v_mov_b32_e32 v2, v4
	v_mov_b32_e32 v1, v6
	s_or_b64 exec, exec, s[6:7]
	v_mov_b32_dpp v4, v5 quad_perm:[2,3,0,1] row_mask:0xf bank_mask:0xf bound_ctrl:1
	v_mov_b32_dpp v6, v1 quad_perm:[2,3,0,1] row_mask:0xf bank_mask:0xf bound_ctrl:1
	v_cmp_lt_f32_e64 s[4:5], v2, v4
	v_cmp_nlt_f32_e32 vcc, v2, v4
	s_and_saveexec_b64 s[6:7], vcc
	v_cmp_eq_f32_e32 vcc, v2, v4
	v_cmp_lt_i32_e64 s[46:47], v6, v1
	s_and_b64 s[12:13], vcc, s[46:47]
	s_andn2_b64 s[4:5], s[4:5], exec
	s_and_b64 s[12:13], s[12:13], exec
	s_or_b64 s[4:5], s[4:5], s[12:13]
	s_or_b64 exec, exec, s[6:7]
	s_and_saveexec_b64 s[6:7], s[4:5]
	v_mov_b32_e32 v5, v4
	v_mov_b32_e32 v2, v4
	v_mov_b32_e32 v1, v6
	s_or_b64 exec, exec, s[6:7]
	v_mov_b32_dpp v4, v5 row_half_mirror row_mask:0xf bank_mask:0xf bound_ctrl:1
	v_mov_b32_dpp v6, v1 row_half_mirror row_mask:0xf bank_mask:0xf bound_ctrl:1
	v_cmp_lt_f32_e64 s[4:5], v2, v4
	v_cmp_nlt_f32_e32 vcc, v2, v4
	s_and_saveexec_b64 s[6:7], vcc
	v_cmp_eq_f32_e32 vcc, v2, v4
	v_cmp_lt_i32_e64 s[46:47], v6, v1
	s_and_b64 s[12:13], vcc, s[46:47]
	s_andn2_b64 s[4:5], s[4:5], exec
	s_and_b64 s[12:13], s[12:13], exec
	s_or_b64 s[4:5], s[4:5], s[12:13]
	s_or_b64 exec, exec, s[6:7]
	s_and_saveexec_b64 s[6:7], s[4:5]
	v_mov_b32_e32 v5, v4
	v_mov_b32_e32 v2, v4
	v_mov_b32_e32 v1, v6
	s_or_b64 exec, exec, s[6:7]
	v_mov_b32_dpp v4, v5 row_mirror row_mask:0xf bank_mask:0xf bound_ctrl:1
	v_mov_b32_dpp v6, v1 row_mirror row_mask:0xf bank_mask:0xf bound_ctrl:1
	v_cmp_lt_f32_e64 s[4:5], v2, v4
	v_cmp_nlt_f32_e32 vcc, v2, v4
	s_and_saveexec_b64 s[6:7], vcc
	v_cmp_eq_f32_e32 vcc, v2, v4
	v_cmp_lt_i32_e64 s[46:47], v6, v1
	s_and_b64 s[12:13], vcc, s[46:47]
	s_andn2_b64 s[4:5], s[4:5], exec
	s_and_b64 s[12:13], s[12:13], exec
	s_or_b64 s[4:5], s[4:5], s[12:13]
	s_or_b64 exec, exec, s[6:7]
	s_and_saveexec_b64 s[6:7], s[4:5]
	v_mov_b32_e32 v5, v4
	v_mov_b32_e32 v2, v4
	v_mov_b32_e32 v1, v6
	s_or_b64 exec, exec, s[6:7]
	v_mov_b32_e32 v106, v5
	v_mov_b32_e32 v107, v1
	v_mov_b32_e32 v108, v5
	v_mov_b32_e32 v109, v1
	s_nop 1
	v_permlane16_swap_b32_e32 v106, v108
	v_permlane16_swap_b32_e32 v107, v109
	v_cndmask_b32_e64 v5, v106, v108, s[70:71]
	v_cndmask_b32_e64 v4, v107, v109, s[70:71]
	s_waitcnt lgkmcnt(1)
	v_cmp_lt_f32_e64 s[4:5], v2, v5
	v_cmp_nlt_f32_e32 vcc, v2, v5
	s_and_saveexec_b64 s[6:7], vcc
	s_cbranch_execz .LBB0_981
	v_cmp_eq_f32_e32 vcc, v2, v5
	s_waitcnt lgkmcnt(0)
	v_cmp_lt_i32_e64 s[46:47], v4, v1
	s_and_b64 s[12:13], vcc, s[46:47]
	s_andn2_b64 s[4:5], s[4:5], exec
	s_and_b64 s[12:13], s[12:13], exec
	s_or_b64 s[4:5], s[4:5], s[12:13]

; DI int shfl_src(int x, int src_lane) { return __builtin_amdgcn_ds_bpermute(src_lane << 2, x); }
; DI void phase_tail(const Frame& F, int l) {
;     ...
;             for (int k = 0; k < 4; ++k) { float v = mylogit; int idx = r;
; #pragma unroll
;                 for (int st = 0; st < 5; ++st) { float ov; int oi;
;                     if (st == 0) { ov = __builtin_bit_cast(float, __builtin_amdgcn_update_dpp(0, __builtin_bit_cast(int, v), 0xB1, 0xf, 0xf, true)); oi = __builtin_amdgcn_update_dpp(0, idx, 0xB1, 0xf, 0xf, true); }
;                     else if (st == 1) { ov = __builtin_bit_cast(float, __builtin_amdgcn_update_dpp(0, __builtin_bit_cast(int, v), 0x4E, 0xf, 0xf, true)); oi = __builtin_amdgcn_update_dpp(0, idx, 0x4E, 0xf, 0xf, true); }
;                     else if (st == 2) { ov = __builtin_bit_cast(float, __builtin_amdgcn_update_dpp(0, __builtin_bit_cast(int, v), 0x141, 0xf, 0xf, true)); oi = __builtin_amdgcn_update_dpp(0, idx, 0x141, 0xf, 0xf, true); }
;                     else if (st == 3) { ov = __builtin_bit_cast(float, __builtin_amdgcn_update_dpp(0, __builtin_bit_cast(int, v), 0x140, 0xf, 0xf, true)); oi = __builtin_amdgcn_update_dpp(0, idx, 0x140, 0xf, 0xf, true); }
;                     else { ov = __builtin_bit_cast(float, shfl_src(__builtin_bit_cast(int, v), F.lane ^ 16)); oi = shfl_src(idx, F.lane ^ 16); }
;                     if (ov > v || (ov == v && oi < idx)) { v = ov; idx = oi; } }
;                 tv[k] = v; tix[k] = idx; if (r == idx) mylogit = neg_big; }
.LBB0_983:
	s_or_b64 exec, exec, s[6:7]
	v_cmp_eq_u32_e32 vcc, v67, v1
	v_mov_b32_dpp v8, v67 quad_perm:[1,0,3,2] row_mask:0xf bank_mask:0xf bound_ctrl:1
	s_nop 0
	v_cndmask_b32_e32 v5, v3, v136, vcc
	s_nop 1
	v_mov_b32_dpp v7, v5 quad_perm:[1,0,3,2] row_mask:0xf bank_mask:0xf bound_ctrl:1
	v_cmp_lt_f32_e64 s[4:5], v5, v7
	v_cmp_nlt_f32_e32 vcc, v5, v7
	s_and_saveexec_b64 s[6:7], vcc
	v_cmp_eq_f32_e32 vcc, v5, v7
	v_cmp_lt_i32_e64 s[46:47], v8, v67
	s_and_b64 s[12:13], vcc, s[46:47]
	s_andn2_b64 s[4:5], s[4:5], exec
	s_and_b64 s[12:13], s[12:13], exec
	s_or_b64 s[4:5], s[4:5], s[12:13]
	s_or_b64 exec, exec, s[6:7]
	v_mov_b32_e32 v6, v5
	s_waitcnt lgkmcnt(0)
	v_mov_b32_e32 v4, v5
	v_mov_b32_e32 v3, v67
	s_and_saveexec_b64 s[6:7], s[4:5]
	v_mov_b32_e32 v6, v7
	v_mov_b32_e32 v4, v7
	v_mov_b32_e32 v3, v8
	s_or_b64 exec, exec, s[6:7]
	v_mov_b32_dpp v7, v6 quad_perm:[2,3,0,1] row_mask:0xf bank_mask:0xf bound_ctrl:1
	v_mov_b32_dpp v8, v3 quad_perm:[2,3,0,1] row_mask:0xf bank_mask:0xf bound_ctrl:1
	v_cmp_lt_f32_e64 s[4:5], v4, v7
	v_cmp_nlt_f32_e32 vcc, v4, v7
	s_and_saveexec_b64 s[6:7], vcc
	v_cmp_eq_f32_e32 vcc, v4, v7
	v_cmp_lt_i32_e64 s[46:47], v8, v3
	s_and_b64 s[12:13], vcc, s[46:47]
	s_andn2_b64 s[4:5], s[4:5], exec
	s_and_b64 s[12:13], s[12:13], exec
	s_or_b64 s[4:5], s[4:5], s[12:13]
	s_or_b64 exec, exec, s[6:7]
	s_and_saveexec_b64 s[6:7], s[4:5]
	v_mov_b32_e32 v6, v7
	v_mov_b32_e32 v4, v7
	v_mov_b32_e32 v3, v8
	s_or_b64 exec, exec, s[6:7]
	v_mov_b32_dpp v7, v6 row_half_mirror row_mask:0xf bank_mask:0xf bound_ctrl:1
	v_mov_b32_dpp v8, v3 row_half_mirror row_mask:0xf bank_mask:0xf bound_ctrl:1
	v_cmp_lt_f32_e64 s[4:5], v4, v7
	v_cmp_nlt_f32_e32 vcc, v4, v7
	s_and_saveexec_b64 s[6:7], vcc
	v_cmp_eq_f32_e32 vcc, v4, v7
	v_cmp_lt_i32_e64 s[46:47], v8, v3
	s_and_b64 s[12:13], vcc, s[46:47]
	s_andn2_b64 s[4:5], s[4:5], exec
	s_and_b64 s[12:13], s[12:13], exec
	s_or_b64 s[4:5], s[4:5], s[12:13]
	s_or_b64 exec, exec, s[6:7]
	s_and_saveexec_b64 s[6:7], s[4:5]
	v_mov_b32_e32 v6, v7
	v_mov_b32_e32 v4, v7
	v_mov_b32_e32 v3, v8
	s_or_b64 exec, exec, s[6:7]
	v_mov_b32_dpp v7, v6 row_mirror row_mask:0xf bank_mask:0xf bound_ctrl:1
	v_mov_b32_dpp v8, v3 row_mirror row_mask:0xf bank_mask:0xf bound_ctrl:1
	v_cmp_lt_f32_e64 s[4:5], v4, v7
	v_cmp_nlt_f32_e32 vcc, v4, v7
	s_and_saveexec_b64 s[6:7], vcc
	v_cmp_eq_f32_e32 vcc, v4, v7
	v_cmp_lt_i32_e64 s[46:47], v8, v3
	s_and_b64 s[12:13], vcc, s[46:47]
	s_andn2_b64 s[4:5], s[4:5], exec
	s_and_b64 s[12:13], s[12:13], exec
	s_or_b64 s[4:5], s[4:5], s[12:13]
	s_or_b64 exec, exec, s[6:7]
	s_and_saveexec_b64 s[6:7], s[4:5]
	v_mov_b32_e32 v6, v7
	v_mov_b32_e32 v4, v7
	v_mov_b32_e32 v3, v8
	s_or_b64 exec, exec, s[6:7]
	v_mov_b32_e32 v106, v6
	v_mov_b32_e32 v107, v3
	v_mov_b32_e32 v108, v6
	v_mov_b32_e32 v109, v3
	s_nop 1
	v_permlane16_swap_b32_e32 v106, v108
	v_permlane16_swap_b32_e32 v107, v109
	v_cndmask_b32_e64 v7, v106, v108, s[70:71]
	v_cndmask_b32_e64 v6, v107, v109, s[70:71]
	s_waitcnt lgkmcnt(1)
	v_cmp_lt_f32_e64 s[4:5], v4, v7
	v_cmp_nlt_f32_e32 vcc, v4, v7
	s_and_saveexec_b64 s[6:7], vcc
	s_cbranch_execz .LBB0_1001
	v_cmp_eq_f32_e32 vcc, v4, v7
	s_waitcnt lgkmcnt(0)
	v_cmp_lt_i32_e64 s[46:47], v6, v3
	s_and_b64 s[12:13], vcc, s[46:47]
	s_andn2_b64 s[4:5], s[4:5], exec
	s_and_b64 s[12:13], s[12:13], exec
	s_or_b64 s[4:5], s[4:5], s[12:13]

; DI int shfl_src(int x, int src_lane) { return __builtin_amdgcn_ds_bpermute(src_lane << 2, x); }
; DI void phase_tail(const Frame& F, int l) {
;     ...
;             for (int k = 0; k < 4; ++k) { float v = mylogit; int idx = r;
; #pragma unroll
;                 for (int st = 0; st < 5; ++st) { float ov; int oi;
;                     if (st == 0) { ov = __builtin_bit_cast(float, __builtin_amdgcn_update_dpp(0, __builtin_bit_cast(int, v), 0xB1, 0xf, 0xf, true)); oi = __builtin_amdgcn_update_dpp(0, idx, 0xB1, 0xf, 0xf, true); }
;                     else if (st == 1) { ov = __builtin_bit_cast(float, __builtin_amdgcn_update_dpp(0, __builtin_bit_cast(int, v), 0x4E, 0xf, 0xf, true)); oi = __builtin_amdgcn_update_dpp(0, idx, 0x4E, 0xf, 0xf, true); }
;                     else if (st == 2) { ov = __builtin_bit_cast(float, __builtin_amdgcn_update_dpp(0, __builtin_bit_cast(int, v), 0x141, 0xf, 0xf, true)); oi = __builtin_amdgcn_update_dpp(0, idx, 0x141, 0xf, 0xf, true); }
;                     else if (st == 3) { ov = __builtin_bit_cast(float, __builtin_amdgcn_update_dpp(0, __builtin_bit_cast(int, v), 0x140, 0xf, 0xf, true)); oi = __builtin_amdgcn_update_dpp(0, idx, 0x140, 0xf, 0xf, true); }
;                     else { ov = __builtin_bit_cast(float, shfl_src(__builtin_bit_cast(int, v), F.lane ^ 16)); oi = shfl_src(idx, F.lane ^ 16); }
;                     if (ov > v || (ov == v && oi < idx)) { v = ov; idx = oi; } }
;                 tv[k] = v; tix[k] = idx; if (r == idx) mylogit = neg_big; }
.LBB0_1003:
	s_or_b64 exec, exec, s[6:7]
	v_cmp_eq_u32_e32 vcc, v67, v3
	v_mov_b32_dpp v10, v67 quad_perm:[1,0,3,2] row_mask:0xf bank_mask:0xf bound_ctrl:1
	s_nop 0
	v_cndmask_b32_e32 v7, v5, v136, vcc
	s_nop 1
	v_mov_b32_dpp v9, v7 quad_perm:[1,0,3,2] row_mask:0xf bank_mask:0xf bound_ctrl:1
	v_cmp_lt_f32_e64 s[4:5], v7, v9
	v_cmp_nlt_f32_e32 vcc, v7, v9
	s_and_saveexec_b64 s[6:7], vcc
	v_cmp_eq_f32_e32 vcc, v7, v9
	v_cmp_lt_i32_e64 s[46:47], v10, v67
	s_and_b64 s[12:13], vcc, s[46:47]
	s_andn2_b64 s[4:5], s[4:5], exec
	s_and_b64 s[12:13], s[12:13], exec
	s_or_b64 s[4:5], s[4:5], s[12:13]
	s_or_b64 exec, exec, s[6:7]
	v_mov_b32_e32 v8, v7
	s_waitcnt lgkmcnt(0)
	v_mov_b32_e32 v6, v7
	v_mov_b32_e32 v5, v67
	s_and_saveexec_b64 s[6:7], s[4:5]
	v_mov_b32_e32 v8, v9
	v_mov_b32_e32 v6, v9
	v_mov_b32_e32 v5, v10
	s_or_b64 exec, exec, s[6:7]
	v_mov_b32_dpp v9, v8 quad_perm:[2,3,0,1] row_mask:0xf bank_mask:0xf bound_ctrl:1
	v_mov_b32_dpp v10, v5 quad_perm:[2,3,0,1] row_mask:0xf bank_mask:0xf bound_ctrl:1
	v_cmp_lt_f32_e64 s[4:5], v6, v9
	v_cmp_nlt_f32_e32 vcc, v6, v9
	s_and_saveexec_b64 s[6:7], vcc
	v_cmp_eq_f32_e32 vcc, v6, v9
	v_cmp_lt_i32_e64 s[46:47], v10, v5
	s_and_b64 s[12:13], vcc, s[46:47]
	s_andn2_b64 s[4:5], s[4:5], exec
	s_and_b64 s[12:13], s[12:13], exec
	s_or_b64 s[4:5], s[4:5], s[12:13]
	s_or_b64 exec, exec, s[6:7]
	s_and_saveexec_b64 s[6:7], s[4:5]
	v_mov_b32_e32 v8, v9
	v_mov_b32_e32 v6, v9
	v_mov_b32_e32 v5, v10
	s_or_b64 exec, exec, s[6:7]
	v_mov_b32_dpp v9, v8 row_half_mirror row_mask:0xf bank_mask:0xf bound_ctrl:1
	v_mov_b32_dpp v10, v5 row_half_mirror row_mask:0xf bank_mask:0xf bound_ctrl:1
	v_cmp_lt_f32_e64 s[4:5], v6, v9
	v_cmp_nlt_f32_e32 vcc, v6, v9
	s_and_saveexec_b64 s[6:7], vcc
	v_cmp_eq_f32_e32 vcc, v6, v9
	v_cmp_lt_i32_e64 s[46:47], v10, v5
	s_and_b64 s[12:13], vcc, s[46:47]
	s_andn2_b64 s[4:5], s[4:5], exec
	s_and_b64 s[12:13], s[12:13], exec
	s_or_b64 s[4:5], s[4:5], s[12:13]
	s_or_b64 exec, exec, s[6:7]
	s_and_saveexec_b64 s[6:7], s[4:5]
	v_mov_b32_e32 v8, v9
	v_mov_b32_e32 v6, v9
	v_mov_b32_e32 v5, v10
	s_or_b64 exec, exec, s[6:7]
	v_mov_b32_dpp v9, v8 row_mirror row_mask:0xf bank_mask:0xf bound_ctrl:1
	v_mov_b32_dpp v10, v5 row_mirror row_mask:0xf bank_mask:0xf bound_ctrl:1
	v_cmp_lt_f32_e64 s[4:5], v6, v9
	v_cmp_nlt_f32_e32 vcc, v6, v9
	s_and_saveexec_b64 s[6:7], vcc
	v_cmp_eq_f32_e32 vcc, v6, v9
	v_cmp_lt_i32_e64 s[46:47], v10, v5
	s_and_b64 s[12:13], vcc, s[46:47]
	s_andn2_b64 s[4:5], s[4:5], exec
	s_and_b64 s[12:13], s[12:13], exec
	s_or_b64 s[4:5], s[4:5], s[12:13]
	s_or_b64 exec, exec, s[6:7]
	s_and_saveexec_b64 s[6:7], s[4:5]
	v_mov_b32_e32 v8, v9
	v_mov_b32_e32 v6, v9
	v_mov_b32_e32 v5, v10
	s_or_b64 exec, exec, s[6:7]
	v_mov_b32_e32 v106, v8
	v_mov_b32_e32 v107, v5
	v_mov_b32_e32 v108, v8
	v_mov_b32_e32 v109, v5
	s_nop 1
	v_permlane16_swap_b32_e32 v106, v108
	v_permlane16_swap_b32_e32 v107, v109
	v_cndmask_b32_e64 v9, v106, v108, s[70:71]
	v_cndmask_b32_e64 v8, v107, v109, s[70:71]
	s_waitcnt lgkmcnt(1)
	v_cmp_lt_f32_e64 s[4:5], v6, v9
	v_cmp_nlt_f32_e32 vcc, v6, v9
	s_and_saveexec_b64 s[6:7], vcc
	s_cbranch_execz .LBB0_1021
	v_cmp_eq_f32_e32 vcc, v6, v9
	s_waitcnt lgkmcnt(0)
	v_cmp_lt_i32_e64 s[46:47], v8, v5
	s_and_b64 s[12:13], vcc, s[46:47]
	s_andn2_b64 s[4:5], s[4:5], exec
	s_and_b64 s[12:13], s[12:13], exec
	s_or_b64 s[4:5], s[4:5], s[12:13]

; DI int shfl_src(int x, int src_lane) { return __builtin_amdgcn_ds_bpermute(src_lane << 2, x); }
; DI void phase_tail(const Frame& F, int l) {
;     ...
;             for (int k = 0; k < 4; ++k) { float v = mylogit; int idx = r;
; #pragma unroll
;                 for (int st = 0; st < 5; ++st) { float ov; int oi;
;                     if (st == 0) { ov = __builtin_bit_cast(float, __builtin_amdgcn_update_dpp(0, __builtin_bit_cast(int, v), 0xB1, 0xf, 0xf, true)); oi = __builtin_amdgcn_update_dpp(0, idx, 0xB1, 0xf, 0xf, true); }
;                     else if (st == 1) { ov = __builtin_bit_cast(float, __builtin_amdgcn_update_dpp(0, __builtin_bit_cast(int, v), 0x4E, 0xf, 0xf, true)); oi = __builtin_amdgcn_update_dpp(0, idx, 0x4E, 0xf, 0xf, true); }
;                     else if (st == 2) { ov = __builtin_bit_cast(float, __builtin_amdgcn_update_dpp(0, __builtin_bit_cast(int, v), 0x141, 0xf, 0xf, true)); oi = __builtin_amdgcn_update_dpp(0, idx, 0x141, 0xf, 0xf, true); }
;                     else if (st == 3) { ov = __builtin_bit_cast(float, __builtin_amdgcn_update_dpp(0, __builtin_bit_cast(int, v), 0x140, 0xf, 0xf, true)); oi = __builtin_amdgcn_update_dpp(0, idx, 0x140, 0xf, 0xf, true); }
;                     else { ov = __builtin_bit_cast(float, shfl_src(__builtin_bit_cast(int, v), F.lane ^ 16)); oi = shfl_src(idx, F.lane ^ 16); }
;                     if (ov > v || (ov == v && oi < idx)) { v = ov; idx = oi; } }
;                 tv[k] = v; tix[k] = idx; if (r == idx) mylogit = neg_big; }
.LBB0_1023:
	s_or_b64 exec, exec, s[6:7]
	v_cmp_eq_u32_e32 vcc, v67, v5
	v_mov_b32_dpp v9, v67 quad_perm:[1,0,3,2] row_mask:0xf bank_mask:0xf bound_ctrl:1
	s_nop 0
	v_cndmask_b32_e32 v7, v7, v136, vcc
	s_nop 1
	v_mov_b32_dpp v10, v7 quad_perm:[1,0,3,2] row_mask:0xf bank_mask:0xf bound_ctrl:1
	v_cmp_lt_f32_e64 s[4:5], v7, v10
	v_cmp_nlt_f32_e32 vcc, v7, v10
	s_and_saveexec_b64 s[6:7], vcc
	v_cmp_eq_f32_e32 vcc, v7, v10
	v_cmp_lt_i32_e64 s[46:47], v9, v67
	s_and_b64 s[12:13], vcc, s[46:47]
	s_andn2_b64 s[4:5], s[4:5], exec
	s_and_b64 s[12:13], s[12:13], exec
	s_or_b64 s[4:5], s[4:5], s[12:13]
	s_or_b64 exec, exec, s[6:7]
	s_waitcnt lgkmcnt(0)
	v_mov_b32_e32 v8, v67
	s_and_saveexec_b64 s[6:7], s[4:5]
	v_mov_b32_e32 v7, v10
	v_mov_b32_e32 v8, v9
	s_or_b64 exec, exec, s[6:7]
	v_mov_b32_dpp v10, v7 quad_perm:[2,3,0,1] row_mask:0xf bank_mask:0xf bound_ctrl:1
	v_mov_b32_dpp v9, v8 quad_perm:[2,3,0,1] row_mask:0xf bank_mask:0xf bound_ctrl:1
	v_cmp_lt_f32_e64 s[4:5], v7, v10
	v_cmp_nlt_f32_e32 vcc, v7, v10
	s_and_saveexec_b64 s[6:7], vcc
	v_cmp_eq_f32_e32 vcc, v7, v10
	v_cmp_lt_i32_e64 s[46:47], v9, v8
	s_and_b64 s[12:13], vcc, s[46:47]
	s_andn2_b64 s[4:5], s[4:5], exec
	s_and_b64 s[12:13], s[12:13], exec
	s_or_b64 s[4:5], s[4:5], s[12:13]
	s_or_b64 exec, exec, s[6:7]
	s_and_saveexec_b64 s[6:7], s[4:5]
	v_mov_b32_e32 v7, v10
	v_mov_b32_e32 v8, v9
	s_or_b64 exec, exec, s[6:7]
	v_mov_b32_dpp v10, v7 row_half_mirror row_mask:0xf bank_mask:0xf bound_ctrl:1
	v_mov_b32_dpp v9, v8 row_half_mirror row_mask:0xf bank_mask:0xf bound_ctrl:1
	v_cmp_lt_f32_e64 s[4:5], v7, v10
	v_cmp_nlt_f32_e32 vcc, v7, v10
	s_and_saveexec_b64 s[6:7], vcc
	v_cmp_eq_f32_e32 vcc, v7, v10
	v_cmp_lt_i32_e64 s[46:47], v9, v8
	s_and_b64 s[12:13], vcc, s[46:47]
	s_andn2_b64 s[4:5], s[4:5], exec
	s_and_b64 s[12:13], s[12:13], exec
	s_or_b64 s[4:5], s[4:5], s[12:13]
	s_or_b64 exec, exec, s[6:7]
	s_and_saveexec_b64 s[6:7], s[4:5]
	v_mov_b32_e32 v7, v10
	v_mov_b32_e32 v8, v9
	s_or_b64 exec, exec, s[6:7]
	v_mov_b32_dpp v10, v7 row_mirror row_mask:0xf bank_mask:0xf bound_ctrl:1
	v_mov_b32_dpp v9, v8 row_mirror row_mask:0xf bank_mask:0xf bound_ctrl:1
	v_cmp_lt_f32_e64 s[4:5], v7, v10
	v_cmp_nlt_f32_e32 vcc, v7, v10
	s_and_saveexec_b64 s[6:7], vcc
	v_cmp_eq_f32_e32 vcc, v7, v10
	v_cmp_lt_i32_e64 s[46:47], v9, v8
	s_and_b64 s[12:13], vcc, s[46:47]
	s_andn2_b64 s[4:5], s[4:5], exec
	s_and_b64 s[12:13], s[12:13], exec
	s_or_b64 s[4:5], s[4:5], s[12:13]
	s_or_b64 exec, exec, s[6:7]
	s_and_saveexec_b64 s[6:7], s[4:5]
	v_mov_b32_e32 v7, v10
	v_mov_b32_e32 v8, v9
	s_or_b64 exec, exec, s[6:7]
	v_mov_b32_e32 v106, v7
	v_mov_b32_e32 v107, v8
	v_mov_b32_e32 v108, v7
	v_mov_b32_e32 v109, v8
	s_nop 1
	v_permlane16_swap_b32_e32 v106, v108
	v_permlane16_swap_b32_e32 v107, v109
	v_cndmask_b32_e64 v10, v106, v108, s[70:71]
	v_cndmask_b32_e64 v9, v107, v109, s[70:71]
	s_waitcnt lgkmcnt(1)
	v_cmp_lt_f32_e64 s[4:5], v7, v10
	v_cmp_nlt_f32_e32 vcc, v7, v10
	s_and_saveexec_b64 s[6:7], vcc
	s_cbranch_execnz .LBB0_1042
	s_or_b64 exec, exec, s[6:7]
	s_and_saveexec_b64 s[6:7], s[4:5]
	s_cbranch_execnz .LBB0_1043
